# epilogue load hoists + P1 K-loop LDS-DMA addresses in saddr form (no 64-bit VALU adds in load segments)
# speedup vs baseline: 1.0061x; 1.0030x over previous
; #define PG8_STAGE2(bufoff, gbase, v0, v1) do { \
;         __builtin_amdgcn_global_load_lds((const unsigned*)((const char*)(gbase) + (v0)), (LAS unsigned*)(lds + (bufoff) + ldsw), 16, 0, 0); \
;         __builtin_amdgcn_global_load_lds((const unsigned*)((const char*)(gbase) + (v1)), (LAS unsigned*)(lds + (bufoff) + ldsw + 8192), 16, 0, 0); } while (0)
; #define PG8_STAGE(bufoff, gbase, voff) PG8_STAGE2(bufoff, gbase, (voff)[0], (voff)[1])
; #define PG8_LDA(dst, b, h) do { _Pragma("unroll") for (int m = 0; m < 4; ++m) _Pragma("unroll") for (int k = 0; k < 2; ++k) dst[m][k] = *(const LAS bf16x8*)(lds + PG8_SA(b, h) + aoff + m * 2048 + k * 1024); } while (0)
; #define PG8_LDB(dst, b, h) do { _Pragma("unroll") for (int n = 0; n < 2; ++n) _Pragma("unroll") for (int k = 0; k < 2; ++k) dst[n][k] = *(const LAS bf16x8*)(lds + PG8_SB(b, h) + boff + n * 2048 + k * 1024); } while (0)
; #define PG8_WAIT_V(n) asm volatile("s_waitcnt vmcnt(" #n ")" ::: "memory")
; #define PG8_WAIT_L(n) asm volatile("s_waitcnt lgkmcnt(" #n ")" ::: "memory")
; #define PG8_BAR __builtin_amdgcn_s_barrier()
; #define PG8_SCHED __builtin_amdgcn_sched_barrier(0)
; template <class Epi, class Sched, bool ALIGN_EPI, bool SP2, bool GATHER>
; DI void gemm_phase(LAS unsigned char* lds, const Gemm g, const Sched& S, const Epi& E) {
;     ...
;             PG8_LDB(B0, 0, 0); PG8_LDB(B1, 0, 1); PG8_SCHED; PG8_LDA(At, 0, 0); PG8_STAGE2(PG8_SA(1, 1), a1 + hstepA, gC[1][0], gC[1][1]);
;             PG8_WAIT_V(8); PG8_WAIT_L(0); PG8_BAR; PG8_MMA(0, 0, At, B0); PG8_MMA(0, 1, At, B1); PG8_BAR; PG8_SCHED;
;             PG8_LDA(At, 0, 1); PG8_STAGE(PG8_SB(0, 0), b2, voffB); PG8_STAGE(PG8_SB(0, 1), b2 + hstep, voffB); PG8_STAGE2(PG8_SA(0, 0), a2, x00, x01);
;             PG8_WAIT_V(8); PG8_WAIT_L(0); PG8_BAR; PG8_MMA(1, 0, At, B0); PG8_MMA(1, 1, At, B1); PG8_BAR; PG8_SCHED;
;             PG8_LDB(B0, 1, 0); PG8_LDB(B1, 1, 1); PG8_SCHED; PG8_LDA(At, 1, 0); PG8_STAGE2(PG8_SA(0, 1), a2 + hstepA, x10, x11);
;             PG8_WAIT_V(8); PG8_WAIT_L(0); PG8_BAR; PG8_MMA(0, 0, At, B0); PG8_MMA(0, 1, At, B1); PG8_BAR; PG8_SCHED;
;             PG8_LDA(At, 1, 1); PG8_STAGE(PG8_SB(1, 0), b3, voffB); PG8_STAGE(PG8_SB(1, 1), b3 + hstep, voffB); PG8_STAGE2(PG8_SA(1, 0), a3, x00, x01);
;             PG8_WAIT_V(8); PG8_WAIT_L(0); PG8_BAR; PG8_MMA(1, 0, At, B0); PG8_MMA(1, 1, At, B1); PG8_BAR; PG8_SCHED;
.LBB0_103:
	ds_read_b128 v[4:7], v175
	ds_read_b128 v[8:11], v175 offset:1024
	ds_read_b128 v[158:161], v175 offset:2048
	ds_read_b128 v[162:165], v175 offset:3072
	ds_read_b128 v[166:169], v176
	ds_read_b128 v[180:183], v176 offset:1024
	ds_read_b128 v[184:187], v176 offset:2048
	ds_read_b128 v[188:191], v176 offset:3072
	s_add_u32 s12, s10, 0xfff80080
	s_addc_u32 s13, s11, -1
	s_cmp_eq_u32 s39, 28
	s_cselect_b32 s15, s5, s13
	s_cselect_b32 s14, s7, s12
	s_cselect_b32 s13, s16, s38
	s_cselect_b32 s12, s17, s22
	s_add_i32 m0, s67, 0xc000
	ds_read_b128 v[192:195], v177
	ds_read_b128 v[196:199], v177 offset:1024
	ds_read_b128 v[200:203], v177 offset:2048
	ds_read_b128 v[204:207], v177 offset:3072
	ds_read_b128 v[208:211], v177 offset:4096
	ds_read_b128 v[212:215], v177 offset:5120
	ds_read_b128 v[216:219], v177 offset:6144
	ds_read_b128 v[220:223], v177 offset:7168
	global_load_lds_dwordx4 v150, s[10:11]
	s_add_i32 m0, s67, 0xe000
	s_nop 0
	global_load_lds_dwordx4 v152, s[10:11]
	s_waitcnt vmcnt(8)
	s_waitcnt lgkmcnt(0)
	s_barrier
	s_setprio 1
	s_waitcnt lgkmcnt(0)
	v_mfma_f32_16x16x32_bf16 v[136:139], v[4:7], v[192:195], v[136:139]
	v_mfma_f32_16x16x32_bf16 v[132:135], v[158:161], v[192:195], v[132:135]
	v_mfma_f32_16x16x32_bf16 v[128:131], v[4:7], v[200:203], v[128:131]
	v_mfma_f32_16x16x32_bf16 v[124:127], v[158:161], v[200:203], v[124:127]
	v_mfma_f32_16x16x32_bf16 v[120:123], v[4:7], v[208:211], v[120:123]
	v_mfma_f32_16x16x32_bf16 v[116:119], v[158:161], v[208:211], v[116:119]
	v_mfma_f32_16x16x32_bf16 v[112:115], v[4:7], v[216:219], v[112:115]
	v_mfma_f32_16x16x32_bf16 v[108:111], v[158:161], v[216:219], v[108:111]
	v_mfma_f32_16x16x32_bf16 v[136:139], v[8:11], v[196:199], v[136:139]
	v_mfma_f32_16x16x32_bf16 v[132:135], v[162:165], v[196:199], v[132:135]
	v_mfma_f32_16x16x32_bf16 v[128:131], v[8:11], v[204:207], v[128:131]
	v_mfma_f32_16x16x32_bf16 v[124:127], v[162:165], v[204:207], v[124:127]
	v_mfma_f32_16x16x32_bf16 v[120:123], v[8:11], v[212:215], v[120:123]
	v_mfma_f32_16x16x32_bf16 v[116:119], v[162:165], v[212:215], v[116:119]
	v_mfma_f32_16x16x32_bf16 v[112:115], v[8:11], v[220:223], v[112:115]
	v_mfma_f32_16x16x32_bf16 v[108:111], v[162:165], v[220:223], v[108:111]
	s_setprio 0
	s_setprio 1
	v_mfma_f32_16x16x32_bf16 v[72:75], v[166:169], v[192:195], v[72:75]
	v_mfma_f32_16x16x32_bf16 v[68:71], v[184:187], v[192:195], v[68:71]
	v_mfma_f32_16x16x32_bf16 v[64:67], v[166:169], v[200:203], v[64:67]
	v_mfma_f32_16x16x32_bf16 v[60:63], v[184:187], v[200:203], v[60:63]
	v_mfma_f32_16x16x32_bf16 v[56:59], v[166:169], v[208:211], v[56:59]
	v_mfma_f32_16x16x32_bf16 v[52:55], v[184:187], v[208:211], v[52:55]
	v_mfma_f32_16x16x32_bf16 v[48:51], v[166:169], v[216:219], v[48:51]
	v_mfma_f32_16x16x32_bf16 v[44:47], v[184:187], v[216:219], v[44:47]
	v_mfma_f32_16x16x32_bf16 v[72:75], v[180:183], v[196:199], v[72:75]
	v_mfma_f32_16x16x32_bf16 v[68:71], v[188:191], v[196:199], v[68:71]
	v_mfma_f32_16x16x32_bf16 v[64:67], v[180:183], v[204:207], v[64:67]
	v_mfma_f32_16x16x32_bf16 v[60:63], v[188:191], v[204:207], v[60:63]
	v_mfma_f32_16x16x32_bf16 v[56:59], v[180:183], v[212:215], v[56:59]
	v_mfma_f32_16x16x32_bf16 v[52:55], v[188:191], v[212:215], v[52:55]
	v_mfma_f32_16x16x32_bf16 v[48:51], v[180:183], v[220:223], v[48:51]
	v_mfma_f32_16x16x32_bf16 v[44:47], v[188:191], v[220:223], v[44:47]
	s_setprio 0
	s_barrier
	s_add_i32 s49, s78, s66
	s_add_u32 s98, s12, 0x80
	s_addc_u32 s99, s13, 0
	s_mov_b32 m0, s49
	ds_read_b128 v[192:195], v177 offset:16384
	ds_read_b128 v[196:199], v177 offset:17408
	ds_read_b128 v[200:203], v177 offset:18432
	ds_read_b128 v[204:207], v177 offset:19456
	ds_read_b128 v[208:211], v177 offset:20480
	ds_read_b128 v[212:215], v177 offset:21504
	ds_read_b128 v[216:219], v177 offset:22528
	ds_read_b128 v[220:223], v177 offset:23552
	global_load_lds_dwordx4 v142, s[12:13]
	s_add_i32 m0, s49, 0x2000
	s_add_u32 s56, s12, 0x80000
	s_addc_u32 s57, s13, 0
	s_add_i32 s49, s79, s66
	global_load_lds_dwordx4 v146, s[12:13]
	s_mov_b32 m0, s49
	s_add_u32 s100, s14, 0x80
	s_addc_u32 s101, s15, 0
	global_load_lds_dwordx4 v142, s[56:57]
	s_add_i32 m0, s49, 0x2000
	s_nop 0
	global_load_lds_dwordx4 v146, s[56:57]
	s_mov_b32 m0, s67
	s_nop 0
	global_load_lds_dwordx4 v140, s[14:15]
	s_mov_b32 m0, s68
	s_nop 0
	global_load_lds_dwordx4 v144, s[14:15]
	s_waitcnt vmcnt(8)
	s_waitcnt lgkmcnt(0)
	s_barrier
	s_setprio 1
	s_waitcnt lgkmcnt(0)
	v_mfma_f32_16x16x32_bf16 v[104:107], v[4:7], v[192:195], v[104:107]
	v_mfma_f32_16x16x32_bf16 v[100:103], v[158:161], v[192:195], v[100:103]
	v_mfma_f32_16x16x32_bf16 v[96:99], v[4:7], v[200:203], v[96:99]
	v_mfma_f32_16x16x32_bf16 v[92:95], v[158:161], v[200:203], v[92:95]
	v_mfma_f32_16x16x32_bf16 v[88:91], v[4:7], v[208:211], v[88:91]
	v_mfma_f32_16x16x32_bf16 v[84:87], v[158:161], v[208:211], v[84:87]
	v_mfma_f32_16x16x32_bf16 v[4:7], v[4:7], v[216:219], v[80:83]
	v_mfma_f32_16x16x32_bf16 v[104:107], v[8:11], v[196:199], v[104:107]
	v_mfma_f32_16x16x32_bf16 v[100:103], v[162:165], v[196:199], v[100:103]
	v_mfma_f32_16x16x32_bf16 v[96:99], v[8:11], v[204:207], v[96:99]
	v_mfma_f32_16x16x32_bf16 v[92:95], v[162:165], v[204:207], v[92:95]
	v_mfma_f32_16x16x32_bf16 v[88:91], v[8:11], v[212:215], v[88:91]
	v_mfma_f32_16x16x32_bf16 v[84:87], v[162:165], v[212:215], v[84:87]
	v_mfma_f32_16x16x32_bf16 v[4:7], v[8:11], v[220:223], v[4:7]
	v_mfma_f32_16x16x32_bf16 v[8:11], v[158:161], v[216:219], v[76:79]
	v_mfma_f32_16x16x32_bf16 v[8:11], v[162:165], v[220:223], v[8:11]
	s_setprio 0
	s_setprio 1
	v_mfma_f32_16x16x32_bf16 v[40:43], v[166:169], v[192:195], v[40:43]
	v_mfma_f32_16x16x32_bf16 v[36:39], v[184:187], v[192:195], v[36:39]
	v_mfma_f32_16x16x32_bf16 v[32:35], v[166:169], v[200:203], v[32:35]
	v_mfma_f32_16x16x32_bf16 v[28:31], v[184:187], v[200:203], v[28:31]
	v_mfma_f32_16x16x32_bf16 v[24:27], v[166:169], v[208:211], v[24:27]
	v_mfma_f32_16x16x32_bf16 v[20:23], v[184:187], v[208:211], v[20:23]
	v_mfma_f32_16x16x32_bf16 v[16:19], v[166:169], v[216:219], v[16:19]
	v_mfma_f32_16x16x32_bf16 v[12:15], v[184:187], v[216:219], v[12:15]
	v_mfma_f32_16x16x32_bf16 v[40:43], v[180:183], v[196:199], v[40:43]
	v_mfma_f32_16x16x32_bf16 v[36:39], v[188:191], v[196:199], v[36:39]
	v_mfma_f32_16x16x32_bf16 v[32:35], v[180:183], v[204:207], v[32:35]
	v_mfma_f32_16x16x32_bf16 v[28:31], v[188:191], v[204:207], v[28:31]
	v_mfma_f32_16x16x32_bf16 v[24:27], v[180:183], v[212:215], v[24:27]
	v_mfma_f32_16x16x32_bf16 v[20:23], v[188:191], v[212:215], v[20:23]
	v_mfma_f32_16x16x32_bf16 v[16:19], v[180:183], v[220:223], v[16:19]
	v_mfma_f32_16x16x32_bf16 v[12:15], v[188:191], v[220:223], v[12:15]
	s_setprio 0
	s_barrier
; #define PG8_STAGE2(bufoff, gbase, v0, v1) do { \
;         __builtin_amdgcn_global_load_lds((const unsigned*)((const char*)(gbase) + (v0)), (LAS unsigned*)(lds + (bufoff) + ldsw), 16, 0, 0); \
;         __builtin_amdgcn_global_load_lds((const unsigned*)((const char*)(gbase) + (v1)), (LAS unsigned*)(lds + (bufoff) + ldsw + 8192), 16, 0, 0); } while (0)
; #define PG8_STAGE(bufoff, gbase, voff) PG8_STAGE2(bufoff, gbase, (voff)[0], (voff)[1])
; #define PG8_LDA(dst, b, h) do { _Pragma("unroll") for (int m = 0; m < 4; ++m) _Pragma("unroll") for (int k = 0; k < 2; ++k) dst[m][k] = *(const LAS bf16x8*)(lds + PG8_SA(b, h) + aoff + m * 2048 + k * 1024); } while (0)
; #define PG8_LDB(dst, b, h) do { _Pragma("unroll") for (int n = 0; n < 2; ++n) _Pragma("unroll") for (int k = 0; k < 2; ++k) dst[n][k] = *(const LAS bf16x8*)(lds + PG8_SB(b, h) + boff + n * 2048 + k * 1024); } while (0)
; #define PG8_WAIT_V(n) asm volatile("s_waitcnt vmcnt(" #n ")" ::: "memory")
; #define PG8_WAIT_L(n) asm volatile("s_waitcnt lgkmcnt(" #n ")" ::: "memory")
; #define PG8_BAR __builtin_amdgcn_s_barrier()
; #define PG8_SCHED __builtin_amdgcn_sched_barrier(0)
; template <class Epi, class Sched, bool ALIGN_EPI, bool SP2, bool GATHER>
; DI void gemm_phase(LAS unsigned char* lds, const Gemm g, const Sched& S, const Epi& E) {
;     ...
;             PG8_LDB(B0, 0, 0); PG8_LDB(B1, 0, 1); PG8_SCHED; PG8_LDA(At, 0, 0); PG8_STAGE2(PG8_SA(1, 1), a1 + hstepA, gC[1][0], gC[1][1]);
;             PG8_WAIT_V(8); PG8_WAIT_L(0); PG8_BAR; PG8_MMA(0, 0, At, B0); PG8_MMA(0, 1, At, B1); PG8_BAR; PG8_SCHED;
;             PG8_LDA(At, 0, 1); PG8_STAGE(PG8_SB(0, 0), b2, voffB); PG8_STAGE(PG8_SB(0, 1), b2 + hstep, voffB); PG8_STAGE2(PG8_SA(0, 0), a2, x00, x01);
;             PG8_WAIT_V(8); PG8_WAIT_L(0); PG8_BAR; PG8_MMA(1, 0, At, B0); PG8_MMA(1, 1, At, B1); PG8_BAR; PG8_SCHED;
;             PG8_LDB(B0, 1, 0); PG8_LDB(B1, 1, 1); PG8_SCHED; PG8_LDA(At, 1, 0); PG8_STAGE2(PG8_SA(0, 1), a2 + hstepA, x10, x11);
;             PG8_WAIT_V(8); PG8_WAIT_L(0); PG8_BAR; PG8_MMA(0, 0, At, B0); PG8_MMA(0, 1, At, B1); PG8_BAR; PG8_SCHED;
;             PG8_LDA(At, 1, 1); PG8_STAGE(PG8_SB(1, 0), b3, voffB); PG8_STAGE(PG8_SB(1, 1), b3 + hstep, voffB); PG8_STAGE2(PG8_SA(1, 0), a3, x00, x01);
;             PG8_WAIT_V(8); PG8_WAIT_L(0); PG8_BAR; PG8_MMA(1, 0, At, B0); PG8_MMA(1, 1, At, B1); PG8_BAR; PG8_SCHED;
;         }
	s_add_i32 s49, 0, 0x18000
	v_add_u32_e32 v3, s49, v172
	s_add_i32 s51, 0, 0x1c000
	ds_read_b128 v[76:79], v3
	ds_read_b128 v[80:83], v3 offset:1024
	ds_read_b128 v[158:161], v3 offset:2048
	ds_read_b128 v[162:165], v3 offset:3072
	v_add_u32_e32 v3, s51, v172
	ds_read_b128 v[166:169], v3
	ds_read_b128 v[180:183], v3 offset:1024
	ds_read_b128 v[184:187], v3 offset:2048
	ds_read_b128 v[188:191], v3 offset:3072
	s_add_u32 s14, s14, 0x80000
	s_addc_u32 s15, s15, 0
	s_mov_b32 m0, s69
	ds_read_b128 v[192:195], v177 offset:32768
	ds_read_b128 v[196:199], v177 offset:33792
	ds_read_b128 v[200:203], v177 offset:34816
	ds_read_b128 v[204:207], v177 offset:35840
	ds_read_b128 v[208:211], v177 offset:36864
	ds_read_b128 v[212:215], v177 offset:37888
	ds_read_b128 v[216:219], v177 offset:38912
	ds_read_b128 v[220:223], v177 offset:39936
	global_load_lds_dwordx4 v140, s[14:15]
	s_mov_b32 m0, s70
	s_nop 0
	global_load_lds_dwordx4 v144, s[14:15]
	s_waitcnt vmcnt(8)
	s_waitcnt lgkmcnt(0)
	s_barrier
	s_setprio 1
	s_waitcnt lgkmcnt(0)
	v_mfma_f32_16x16x32_bf16 v[136:139], v[76:79], v[192:195], v[136:139]
	v_mfma_f32_16x16x32_bf16 v[132:135], v[158:161], v[192:195], v[132:135]
	v_mfma_f32_16x16x32_bf16 v[128:131], v[76:79], v[200:203], v[128:131]
	v_mfma_f32_16x16x32_bf16 v[124:127], v[158:161], v[200:203], v[124:127]
	v_mfma_f32_16x16x32_bf16 v[120:123], v[76:79], v[208:211], v[120:123]
	v_mfma_f32_16x16x32_bf16 v[116:119], v[158:161], v[208:211], v[116:119]
	v_mfma_f32_16x16x32_bf16 v[112:115], v[76:79], v[216:219], v[112:115]
	v_mfma_f32_16x16x32_bf16 v[108:111], v[158:161], v[216:219], v[108:111]
	v_mfma_f32_16x16x32_bf16 v[136:139], v[80:83], v[196:199], v[136:139]
	v_mfma_f32_16x16x32_bf16 v[132:135], v[162:165], v[196:199], v[132:135]
	v_mfma_f32_16x16x32_bf16 v[128:131], v[80:83], v[204:207], v[128:131]
	v_mfma_f32_16x16x32_bf16 v[124:127], v[162:165], v[204:207], v[124:127]
	v_mfma_f32_16x16x32_bf16 v[120:123], v[80:83], v[212:215], v[120:123]
	v_mfma_f32_16x16x32_bf16 v[116:119], v[162:165], v[212:215], v[116:119]
	v_mfma_f32_16x16x32_bf16 v[112:115], v[80:83], v[220:223], v[112:115]
	v_mfma_f32_16x16x32_bf16 v[108:111], v[162:165], v[220:223], v[108:111]
	s_setprio 0
	s_setprio 1
	v_mfma_f32_16x16x32_bf16 v[72:75], v[166:169], v[192:195], v[72:75]
	v_mfma_f32_16x16x32_bf16 v[68:71], v[184:187], v[192:195], v[68:71]
	v_mfma_f32_16x16x32_bf16 v[64:67], v[166:169], v[200:203], v[64:67]
	v_mfma_f32_16x16x32_bf16 v[60:63], v[184:187], v[200:203], v[60:63]
	v_mfma_f32_16x16x32_bf16 v[56:59], v[166:169], v[208:211], v[56:59]
	v_mfma_f32_16x16x32_bf16 v[52:55], v[184:187], v[208:211], v[52:55]
	v_mfma_f32_16x16x32_bf16 v[48:51], v[166:169], v[216:219], v[48:51]
	v_mfma_f32_16x16x32_bf16 v[44:47], v[184:187], v[216:219], v[44:47]
	v_mfma_f32_16x16x32_bf16 v[72:75], v[180:183], v[196:199], v[72:75]
	v_mfma_f32_16x16x32_bf16 v[68:71], v[188:191], v[196:199], v[68:71]
	v_mfma_f32_16x16x32_bf16 v[64:67], v[180:183], v[204:207], v[64:67]
	v_mfma_f32_16x16x32_bf16 v[60:63], v[188:191], v[204:207], v[60:63]
	v_mfma_f32_16x16x32_bf16 v[56:59], v[180:183], v[212:215], v[56:59]
	v_mfma_f32_16x16x32_bf16 v[52:55], v[188:191], v[212:215], v[52:55]
	v_mfma_f32_16x16x32_bf16 v[48:51], v[180:183], v[220:223], v[48:51]
	v_mfma_f32_16x16x32_bf16 v[44:47], v[188:191], v[220:223], v[44:47]
	s_setprio 0
	s_barrier
	s_add_i32 s14, s49, s66
	s_mov_b32 m0, s14
	ds_read_b128 v[192:195], v177 offset:49152
	ds_read_b128 v[196:199], v177 offset:50176
	ds_read_b128 v[200:203], v177 offset:51200
	ds_read_b128 v[204:207], v177 offset:52224
	ds_read_b128 v[208:211], v177 offset:53248
	ds_read_b128 v[212:215], v177 offset:54272
	ds_read_b128 v[216:219], v177 offset:55296
	ds_read_b128 v[220:223], v177 offset:56320
	global_load_lds_dwordx4 v142, s[98:99]
	s_add_i32 m0, s14, 0x2000
	s_add_u32 s12, s12, 0x80080
	s_addc_u32 s13, s13, 0
	s_add_i32 s14, s51, s66
	global_load_lds_dwordx4 v146, s[98:99]
	s_mov_b32 m0, s14
	s_nop 0
	global_load_lds_dwordx4 v142, s[12:13]
	s_add_i32 m0, s14, 0x2000
	s_nop 0
	global_load_lds_dwordx4 v146, s[12:13]
	s_mov_b32 m0, s73
	s_nop 0
	global_load_lds_dwordx4 v140, s[100:101]
	s_mov_b32 m0, s74
	s_nop 0
	global_load_lds_dwordx4 v144, s[100:101]
	s_waitcnt vmcnt(8)
	s_waitcnt lgkmcnt(0)
	s_barrier
	s_setprio 1
	s_waitcnt lgkmcnt(0)
	v_mfma_f32_16x16x32_bf16 v[104:107], v[76:79], v[192:195], v[104:107]
	v_mfma_f32_16x16x32_bf16 v[96:99], v[76:79], v[200:203], v[96:99]
	v_mfma_f32_16x16x32_bf16 v[88:91], v[76:79], v[208:211], v[88:91]
	v_mfma_f32_16x16x32_bf16 v[4:7], v[76:79], v[216:219], v[4:7]
	v_mfma_f32_16x16x32_bf16 v[104:107], v[80:83], v[196:199], v[104:107]
	v_mfma_f32_16x16x32_bf16 v[100:103], v[158:161], v[192:195], v[100:103]
	v_mfma_f32_16x16x32_bf16 v[96:99], v[80:83], v[204:207], v[96:99]
	v_mfma_f32_16x16x32_bf16 v[92:95], v[158:161], v[200:203], v[92:95]
	v_mfma_f32_16x16x32_bf16 v[88:91], v[80:83], v[212:215], v[88:91]
	v_mfma_f32_16x16x32_bf16 v[84:87], v[158:161], v[208:211], v[84:87]
	v_mfma_f32_16x16x32_bf16 v[80:83], v[80:83], v[220:223], v[4:7]
	v_mfma_f32_16x16x32_bf16 v[4:7], v[158:161], v[216:219], v[8:11]
	v_mfma_f32_16x16x32_bf16 v[100:103], v[162:165], v[196:199], v[100:103]
	v_mfma_f32_16x16x32_bf16 v[92:95], v[162:165], v[204:207], v[92:95]
	v_mfma_f32_16x16x32_bf16 v[84:87], v[162:165], v[212:215], v[84:87]
	v_mfma_f32_16x16x32_bf16 v[76:79], v[162:165], v[220:223], v[4:7]
	s_setprio 0
	s_setprio 1
	v_mfma_f32_16x16x32_bf16 v[4:7], v[166:169], v[192:195], v[40:43]
	v_mfma_f32_16x16x32_bf16 v[40:43], v[180:183], v[196:199], v[4:7]
	v_mfma_f32_16x16x32_bf16 v[4:7], v[184:187], v[192:195], v[36:39]
	v_mfma_f32_16x16x32_bf16 v[36:39], v[188:191], v[196:199], v[4:7]
	v_mfma_f32_16x16x32_bf16 v[4:7], v[166:169], v[200:203], v[32:35]
	v_mfma_f32_16x16x32_bf16 v[32:35], v[180:183], v[204:207], v[4:7]
	v_mfma_f32_16x16x32_bf16 v[4:7], v[184:187], v[200:203], v[28:31]
	v_mfma_f32_16x16x32_bf16 v[28:31], v[188:191], v[204:207], v[4:7]
	v_mfma_f32_16x16x32_bf16 v[4:7], v[166:169], v[208:211], v[24:27]
	v_mfma_f32_16x16x32_bf16 v[24:27], v[180:183], v[212:215], v[4:7]
	v_mfma_f32_16x16x32_bf16 v[4:7], v[184:187], v[208:211], v[20:23]
	v_mfma_f32_16x16x32_bf16 v[20:23], v[188:191], v[212:215], v[4:7]
	v_mfma_f32_16x16x32_bf16 v[4:7], v[166:169], v[216:219], v[16:19]
	v_mfma_f32_16x16x32_bf16 v[16:19], v[180:183], v[220:223], v[4:7]
	v_mfma_f32_16x16x32_bf16 v[4:7], v[184:187], v[216:219], v[12:15]
	v_mfma_f32_16x16x32_bf16 v[12:15], v[188:191], v[220:223], v[4:7]
	s_setprio 0
	s_barrier
	s_add_i32 s39, s39, 2
	s_add_u32 s10, s10, 0x100
	s_addc_u32 s11, s11, 0
	s_add_u32 s22, s22, 0x100
	s_addc_u32 s38, s38, 0
	s_cmp_gt_u32 s39, 29
	s_cbranch_scc0 .LBB0_103
	s_and_b64 vcc, exec, s[30:31]
	s_cbranch_vccz .LBB0_106
	s_barrier

; __global__ void __launch_bounds__(NTHREADS, 2) fwd(Args args) {
	.amdhsa_kernel _Z3fwd4Args
		.amdhsa_group_segment_fixed_size 0
		.amdhsa_private_segment_fixed_size 0
		.amdhsa_kernarg_size 432
		.amdhsa_user_sgpr_count 2
		.amdhsa_user_sgpr_dispatch_ptr 0
		.amdhsa_user_sgpr_queue_ptr 0
		.amdhsa_user_sgpr_kernarg_segment_ptr 1
		.amdhsa_user_sgpr_dispatch_id 0
		.amdhsa_user_sgpr_kernarg_preload_length 0
		.amdhsa_user_sgpr_kernarg_preload_offset 0
		.amdhsa_user_sgpr_private_segment_size 0
		.amdhsa_uses_dynamic_stack 0
		.amdhsa_enable_private_segment 0
		.amdhsa_system_sgpr_workgroup_id_x 1
		.amdhsa_system_sgpr_workgroup_id_y 0
		.amdhsa_system_sgpr_workgroup_id_z 0
		.amdhsa_system_sgpr_workgroup_info 0
		.amdhsa_system_vgpr_workitem_id 0
		.amdhsa_next_free_vgpr 248
		.amdhsa_next_free_sgpr 102
		.amdhsa_accum_offset 248
		.amdhsa_reserve_vcc 1
		.amdhsa_float_round_mode_32 0
		.amdhsa_float_round_mode_16_64 0
		.amdhsa_float_denorm_mode_32 3
		.amdhsa_float_denorm_mode_16_64 3
		.amdhsa_dx10_clamp 1
		.amdhsa_ieee_mode 1
		.amdhsa_fp16_overflow 0
		.amdhsa_tg_split 0
		.amdhsa_exception_fp_ieee_invalid_op 0
		.amdhsa_exception_fp_denorm_src 0
		.amdhsa_exception_fp_ieee_div_zero 0
		.amdhsa_exception_fp_ieee_overflow 0
		.amdhsa_exception_fp_ieee_underflow 0
		.amdhsa_exception_fp_ieee_inexact 0
		.amdhsa_exception_int_div_zero 0
	.end_amdhsa_kernel

; __global__ void __launch_bounds__(NTHREADS, 2) fwd(Args args) {
amdhsa.kernels:
  - .agpr_count:     0
    .args:
      - .offset:         0
        .size:           176
        .value_kind:     by_value
      - .offset:         176
        .size:           4
        .value_kind:     hidden_block_count_x
      - .offset:         180
        .size:           4
        .value_kind:     hidden_block_count_y
      - .offset:         184
        .size:           4
        .value_kind:     hidden_block_count_z
      - .offset:         188
        .size:           2
        .value_kind:     hidden_group_size_x
      - .offset:         190
        .size:           2
        .value_kind:     hidden_group_size_y
      - .offset:         192
        .size:           2
        .value_kind:     hidden_group_size_z
      - .offset:         194
        .size:           2
        .value_kind:     hidden_remainder_x
      - .offset:         196
        .size:           2
        .value_kind:     hidden_remainder_y
      - .offset:         198
        .size:           2
        .value_kind:     hidden_remainder_z
      - .offset:         216
        .size:           8
        .value_kind:     hidden_global_offset_x
      - .offset:         224
        .size:           8
        .value_kind:     hidden_global_offset_y
      - .offset:         232
        .size:           8
        .value_kind:     hidden_global_offset_z
      - .offset:         240
        .size:           2
        .value_kind:     hidden_grid_dims
      - .offset:         296
        .size:           4
        .value_kind:     hidden_dynamic_lds_size
    .group_segment_fixed_size: 0
    .kernarg_segment_align: 8
    .kernarg_segment_size: 432
    .language:       OpenCL C
    .language_version:
      - 2
      - 0
    .max_flat_workgroup_size: 512
    .name:           _Z3fwd4Args
    .private_segment_fixed_size: 0
    .sgpr_count:     108
    .sgpr_spill_count: 3
    .symbol:         _Z3fwd4Args.kd
    .uniform_work_group_size: 1
    .uses_dynamic_stack: false
    .vgpr_count:     248
    .vgpr_spill_count: 0
    .wavefront_size: 64
